# speedup vs baseline: 1.1157x; 1.0028x over previous
_Z11knrm_kernelPKfS0_PKiS2_S0_Pf:
	s_load_dwordx8 s[4:11], s[0:1], 0x0
	s_load_dwordx4 s[12:15], s[0:1], 0x20
	v_lshrrev_b32_e32 v1, 6, v0
	v_and_b32_e32 v120, 63, v0
	v_lshrrev_b32_e32 v100, 4, v0
	v_and_b32_e32 v123, 15, v0
	v_lshlrev_b32_e32 v124, 5, v1
	s_lshl_b32 s3, s2, 5
	v_lshl_or_b32 v8, s2, 8, v124
	v_or_b32_e32 v2, s3, v100
	s_movk_i32 s3, 0x4b0
	v_mul_lo_u32 v2, v2, s3
	v_mul_lo_u32 v99, v8, s3
	v_lshlrev_b32_e32 v132, 4, v120
	v_min_u32_e32 v193, 23, v120
	v_lshl_add_u32 v3, v123, 4, v2
	v_min_u32_e32 v4, 10, v123
	v_add_u32_e32 v192, v99, v132
	v_lshlrev_b32_e32 v193, 4, v193
	s_movk_i32 s27, 0x1000
	s_movk_i32 s28, 0x2000
	v_lshl_add_u32 v2, v4, 4, v2
	v_add3_u32 v193, v99, v193, s28
	s_mov_b32 s19, 0x20000
	s_mov_b32 s18, 0x4b00000
	s_waitcnt lgkmcnt(0)
	s_mov_b64 s[16:17], s[6:7]
	s_and_b32 s5, s5, 0xffff
	s_mov_b32 s6, 0x960000
	s_mov_b32 s7, s19
	s_and_b32 s17, s17, 0xffff
	buffer_load_dwordx4 v[90:93], v3, s[4:7], 0 offen nt
	buffer_load_dwordx4 v[86:89], v3, s[4:7], 0 offen offset:256 nt
	buffer_load_dwordx4 v[82:85], v3, s[4:7], 0 offen offset:512 nt
	buffer_load_dwordx4 v[78:81], v3, s[4:7], 0 offen offset:768 nt
	buffer_load_dwordx4 v[94:97], v2, s[4:7], 0 offen offset:1024 nt
	buffer_load_dwordx4 v[2:5], v192, s[16:19], 0 offen nt
	buffer_load_dwordx4 v[14:17], v192, s[16:19], 0 offen offset:1024 nt
	buffer_load_dwordx4 v[34:37], v192, s[16:19], 0 offen offset:2048 nt
	buffer_load_dwordx4 v[46:49], v192, s[16:19], 0 offen offset:3072 nt
	buffer_load_dwordx4 v[54:57], v192, s[16:19], s27 offen nt
	buffer_load_dwordx4 v[58:61], v192, s[16:19], s27 offen offset:1024 nt
	buffer_load_dwordx4 v[62:65], v192, s[16:19], s27 offen offset:2048 nt
	buffer_load_dwordx4 v[66:69], v192, s[16:19], s27 offen offset:3072 nt
	buffer_load_dwordx4 v[70:73], v192, s[16:19], s28 offen nt
	buffer_load_dwordx4 v[74:77], v193, s[16:19], 0 offen offset:1024 nt
	v_lshlrev_b32_e32 v42, 2, v0
	v_bfe_u32 v43, v0, 2, 2
	v_and_or_b32 v98, v42, 12, v43
	v_and_or_b32 v6, v98, 7, v8
	v_ashrrev_i32_e32 v7, 31, v6
	s_movk_i32 s0, 0x160
	v_lshl_add_u64 v[6:7], v[6:7], 2, s[10:11]
	v_lshrrev_b32_e32 v121, 5, v0
	v_cmp_gt_u32_e64 s[0:1], s0, v0
	global_load_dword v125, v[6:7], off
	global_load_dword v126, v[6:7], off offset:64
	global_load_dword v127, v[6:7], off offset:96
	global_load_dword v190, v[6:7], off offset:32
	v_cndmask_b32_e64 v42, 10, v121, s[0:1]
	v_lshlrev_b32_e32 v42, 2, v42
	s_lshl_b32 s3, s2, 5
	v_and_b32_e32 v122, 31, v0
	global_load_dword v118, v42, s[12:13]
	v_or_b32_e32 v42, s3, v122
	v_ashrrev_i32_e32 v43, 31, v42
	v_lshl_add_u64 v[42:43], v[42:43], 2, s[8:9]
	global_load_dword v119, v[42:43], off
	s_mov_b32 s3, 0
	v_mul_u32_u24_e32 v131, 0x2600, v1
	v_cmp_gt_u32_e64 s[4:5], 16, v120
	s_and_saveexec_b64 s[6:7], s[4:5]
	s_movk_i32 s8, 0x260
	v_mov_b32_e32 v102, 0
	v_mad_u32_u24 v101, v120, s8, v131
	v_mov_b32_e32 v103, v102
	ds_write_b64 v101, v[102:103] offset:20056
	s_or_b64 exec, exec, s[6:7]
	v_cmp_lt_u32_e32 vcc, 10, v123
	s_waitcnt vmcnt(19)
	v_mul_f32_e32 v101, v87, v87
	v_mov_b32_e32 v106, v92
	s_waitcnt vmcnt(16)
	v_cndmask_b32_e64 v103, v97, 0, vcc
	v_cndmask_b32_e64 v102, v96, 0, vcc
	v_mov_b32_e32 v96, v91
	v_mov_b32_e32 v97, v83
	v_cndmask_b32_e64 v105, v95, 0, vcc
	v_cndmask_b32_e64 v104, v94, 0, vcc
	v_mov_b32_e32 v94, v90
	v_mov_b32_e32 v95, v82
	v_pk_mul_f32 v[96:97], v[96:97], v[96:97]
	v_mov_b32_e32 v107, v84
	v_fmac_f32_e32 v101, v86, v86
	v_pk_fma_f32 v[94:95], v[94:95], v[94:95], v[96:97]
	v_mov_b32_e32 v108, v93
	v_mov_b32_e32 v109, v85
	v_fmac_f32_e32 v101, v88, v88
	v_pk_fma_f32 v[94:95], v[106:107], v[106:107], v[94:95]
	v_fmac_f32_e32 v101, v89, v89
	v_pk_fma_f32 v[94:95], v[108:109], v[108:109], v[94:95]
	v_mov_b32_e32 v96, v79
	v_add_f32_e32 v94, v94, v101
	v_mov_b32_e32 v97, v105
	v_add_f32_e32 v101, v94, v95
	v_mov_b32_e32 v94, v78
	v_mov_b32_e32 v95, v104
	v_pk_mul_f32 v[96:97], v[96:97], v[96:97]
	s_mov_b32 s21, 0xf800000
	v_pk_fma_f32 v[94:95], v[94:95], v[94:95], v[96:97]
	v_mov_b32_e32 v96, v80
	v_mov_b32_e32 v97, v102
	v_pk_fma_f32 v[94:95], v[96:97], v[96:97], v[94:95]
	v_mov_b32_e32 v96, v81
	v_mov_b32_e32 v97, v103
	v_pk_fma_f32 v[94:95], v[96:97], v[96:97], v[94:95]
	v_mov_b32_e32 v135, 0x260
	v_add_f32_e32 v94, v101, v94
	v_add_f32_e32 v94, v94, v95
	v_mbcnt_lo_u32_b32 v95, -1, 0
	v_mbcnt_hi_u32_b32 v95, -1, v95
	v_and_b32_e32 v97, 64, v95
	v_add_u32_e32 v101, 64, v97
	s_movk_i32 s8, 0x260
	v_add_u32_e32 v137, 0x4b00, v99
	s_movk_i32 s10, 0x1b5
	v_mov_b32_e32 v99, 0x36a00
	v_mov_b32_e32 v111, 0x666c0
	v_mov_b32_e32 v113, 0x6d400
	v_mov_b32_e32 v115, 0x74140
	s_mov_b32 s20, 0xbeb17218
	s_mov_b32 s22, 0x44132d1f
	v_mov_b32_e32 v161, 0xc47a0000
	v_add_f32_dpp v96, v94, v94 quad_perm:[1,0,3,2] row_mask:0xf bank_mask:0xf
	s_nop 1
	v_add_f32_dpp v94, v96, v96 quad_perm:[2,3,0,1] row_mask:0xf bank_mask:0xf
	s_nop 1
	v_add_f32_dpp v96, v94, v94 row_half_mirror row_mask:0xf bank_mask:0xf
	s_nop 1
	v_add_f32_dpp v94, v96, v96 row_mirror row_mask:0xf bank_mask:0xf
	v_mul_f32_e32 v96, 0x4f800000, v94
	v_cmp_gt_f32_e32 vcc, s21, v94
	s_nop 1
	v_cndmask_b32_e32 v94, v94, v96, vcc
	v_sqrt_f32_e32 v96, v94
	s_nop 0
	v_add_u32_e32 v106, -1, v96
	v_fma_f32 v107, -v106, v96, v94
	v_cmp_ge_f32_e64 s[6:7], 0, v107
	v_add_u32_e32 v107, 1, v96
	s_nop 0
	v_cndmask_b32_e64 v106, v96, v106, s[6:7]
	v_fma_f32 v96, -v107, v96, v94
	v_cmp_lt_f32_e64 s[6:7], 0, v96
	s_nop 1
	v_cndmask_b32_e64 v96, v106, v107, s[6:7]
	v_mul_f32_e32 v106, 0x37800000, v96
	v_cndmask_b32_e32 v96, v96, v106, vcc
	v_cmp_class_f32_e32 vcc, v94, v135
	s_nop 1
	v_cndmask_b32_e32 v94, v96, v94, vcc
	v_add_f32_e32 v96, 0x29e12e13, v94
	v_div_scale_f32 v106, s[6:7], v96, v96, 1.0
	v_rcp_f32_e32 v107, v106
	v_mov_b32_e32 v94, 0
	v_cmp_gt_u32_e64 s[6:7], 48, v120
	v_mov_b32_e32 v116, v94
	v_fma_f32 v108, -v106, v107, 1.0
	v_fmac_f32_e32 v107, v108, v107
	v_div_scale_f32 v108, vcc, 1.0, v96, 1.0
	v_mul_f32_e32 v109, v108, v107
	v_fma_f32 v110, -v106, v109, v108
	v_fmac_f32_e32 v109, v110, v107
	v_fma_f32 v106, -v106, v109, v108
	v_div_fmas_f32 v106, v106, v107, v109
	v_div_fixup_f32 v96, v106, v96, 1.0
	v_lshlrev_b32_e32 v106, 3, v123
	v_pk_mul_f32 v[82:83], v[96:97], v[82:83] op_sel_hi:[0,1]
	v_pk_mul_f32 v[84:85], v[96:97], v[84:85] op_sel_hi:[0,1]
	v_pk_mul_f32 v[78:79], v[96:97], v[78:79] op_sel_hi:[0,1]
	v_pk_mul_f32 v[80:81], v[96:97], v[80:81] op_sel_hi:[0,1]
	v_mad_u32_u24 v100, v100, s8, v106
	v_cvt_pk_f16_f32 v82, v82, v83
	v_cvt_pk_f16_f32 v83, v84, v85
	v_cvt_pk_f16_f32 v78, v78, v79
	v_cvt_pk_f16_f32 v79, v80, v81
	ds_write2_b64 v100, v[82:83], v[78:79] offset0:32 offset1:48
	v_min_u32_e32 v82, 23, v120
	v_mov_b32_e32 v83, 0x2400
	v_lshl_or_b32 v138, v82, 4, v83
	v_xor_b32_e32 v83, 16, v95
	v_cmp_lt_i32_e32 vcc, v83, v101
	v_pk_mul_f32 v[90:91], v[96:97], v[90:91] op_sel_hi:[0,1]
	v_pk_mul_f32 v[92:93], v[96:97], v[92:93] op_sel_hi:[0,1]
	v_cndmask_b32_e32 v83, v95, v83, vcc
	v_lshlrev_b32_e32 v133, 2, v83
	v_xor_b32_e32 v83, 32, v95
	v_pk_mul_f32 v[86:87], v[96:97], v[86:87] op_sel_hi:[0,1]
	v_pk_mul_f32 v[88:89], v[96:97], v[88:89] op_sel_hi:[0,1]
	v_pk_mul_f32 v[78:79], v[96:97], v[104:105] op_sel_hi:[0,1]
	v_pk_mul_f32 v[80:81], v[96:97], v[102:103] op_sel_hi:[0,1]
	v_cmp_lt_i32_e32 vcc, v83, v101
	v_cvt_pk_f16_f32 v90, v90, v91
	v_cvt_pk_f16_f32 v91, v92, v93
	v_cvt_pk_f16_f32 v86, v86, v87
	v_cvt_pk_f16_f32 v87, v88, v89
	v_cvt_pk_f16_f32 v78, v78, v79
	v_cvt_pk_f16_f32 v79, v80, v81
	v_mov_b32_e32 v81, 0x17c00
	v_cndmask_b32_e32 v83, v95, v83, vcc
	ds_write2_b64 v100, v[90:91], v[86:87] offset1:16
	v_sub_u32_e64 v80, v123, 11 clamp
	v_lshl_or_b32 v81, v1, 7, v81
	v_lshlrev_b32_e32 v134, 2, v83
	v_or_b32_e32 v83, 64, v120
	v_mov_b32_e32 v86, 0x6d40
	v_mov_b32_e32 v87, 0xda80
	v_mov_b32_e32 v89, 0x147c0
	v_mov_b32_e32 v91, 0x1b500
	v_mov_b32_e32 v93, 0x28f80
	v_mov_b32_e32 v96, 0x2fcc0
	v_mov_b32_e32 v101, 0x3d740
	v_mov_b32_e32 v103, 0x44480
	v_mov_b32_e32 v105, 0x4b1c0
	v_mov_b32_e32 v107, 0x58c40
	v_or_b32_e32 v109, 0x3c0, v0
	v_mad_i32_i24 v80, v80, -8, v100
	v_lshrrev_b32_e32 v82, 1, v120
	v_lshl_add_u32 v139, v120, 2, v81
	v_and_or_b32 v140, v120, 48, v81
	v_lshlrev_b32_e32 v81, 3, v120
	v_mul_u32_u24_e32 v84, 0x1b5, v83
	v_lshl_add_u32 v85, v83, 3, v131
	v_mad_u32_u24 v86, v83, s10, v86
	v_mad_u32_u24 v87, v83, s10, v87
	v_mad_u32_u24 v89, v83, s10, v89
	v_mad_u32_u24 v91, v83, s10, v91
	v_mad_u32_u24 v93, v83, s10, v93
	v_mad_u32_u24 v96, v83, s10, v96
	v_mad_u32_u24 v99, v83, s10, v99
	v_mad_u32_u24 v101, v83, s10, v101
	v_mad_u32_u24 v103, v83, s10, v103
	v_mad_u32_u24 v105, v83, s10, v105
	v_mad_u32_u24 v107, v83, s10, v107
	v_mul_u32_u24_e32 v110, 0x1b5, v109
	v_mad_u32_u24 v111, v83, s10, v111
	v_mad_u32_u24 v113, v83, s10, v113
	v_mad_u32_u24 v83, v83, s10, v115
	ds_write_b64 v80, v[78:79] offset:512
	v_mul_u32_u24_e32 v78, 0x260, v123
	v_and_b32_e32 v82, 24, v82
	v_lshrrev_b32_e32 v84, 12, v84
	v_add_u32_e32 v141, v131, v81
	v_lshrrev_b32_e32 v86, 12, v86
	v_lshrrev_b32_e32 v87, 12, v87
	v_lshrrev_b32_e32 v89, 12, v89
	v_lshrrev_b32_e32 v91, 12, v91
	v_lshrrev_b32_e32 v93, 12, v93
	v_lshrrev_b32_e32 v96, 12, v96
	v_lshrrev_b32_e32 v99, 12, v99
	v_lshrrev_b32_e32 v101, 12, v101
	v_lshrrev_b32_e32 v103, 12, v103
	v_lshrrev_b32_e32 v105, 12, v105
	v_lshrrev_b32_e32 v107, 12, v107
	v_lshrrev_b32_e32 v110, 12, v110
	v_lshrrev_b32_e32 v111, 12, v111
	v_lshrrev_b32_e32 v113, 12, v113
	v_lshrrev_b32_e32 v83, 12, v83
	v_and_b32_e32 v79, 48, v0
	v_mad_u32_u24 v80, v98, s8, v131
	v_and_b32_e32 v84, 8, v84
	v_add_u32_e32 v81, 0x400, v141
	v_and_b32_e32 v86, 24, v86
	v_add_u32_e32 v88, 0x600, v141
	v_and_b32_e32 v87, 24, v87
	v_add_u32_e32 v90, 0x800, v141
	v_and_b32_e32 v89, 56, v89
	v_add_u32_e32 v92, 0xa00, v141
	v_and_b32_e32 v91, 56, v91
	v_add_u32_e32 v95, 0xe00, v141
	v_and_b32_e32 v93, 56, v93
	v_add_u32_e32 v98, 0x1000, v141
	v_and_b32_e32 v96, 56, v96
	v_add_u32_e32 v100, 0x1200, v141
	v_and_b32_e32 v99, 0x78, v99
	v_add_u32_e32 v102, 0x1400, v141
	v_and_b32_e32 v101, 0x78, v101
	v_add_u32_e32 v104, 0x1600, v141
	v_and_b32_e32 v103, 0x58, v103
	v_add_u32_e32 v106, 0x1800, v141
	v_and_b32_e32 v105, 0x58, v105
	v_add_u32_e32 v108, 0x1c00, v141
	v_and_b32_e32 v107, 0x78, v107
	v_lshl_add_u32 v109, v109, 3, v131
	v_and_b32_e32 v110, 0x78, v110
	v_add_u32_e32 v112, 0x2000, v141
	v_and_b32_e32 v111, 0x78, v111
	v_add_u32_e32 v114, 0x2200, v141
	v_and_b32_e32 v113, 0x78, v113
	v_add_u32_e32 v115, 0x2400, v141
	v_and_b32_e32 v83, 0xf8, v83
	s_movk_i32 s10, 0x4c00
	v_add_u32_e32 v78, v78, v82
	v_mad_u32_u24 v136, v123, s8, v79
	v_cmp_gt_u32_e64 s[8:9], 24, v120
	v_add3_u32 v142, v80, v79, s10
	v_add_u32_e32 v143, v85, v84
	v_add_u32_e32 v144, v81, v86
	v_add_u32_e32 v145, v88, v87
	v_add_u32_e32 v146, v90, v89
	v_add_u32_e32 v147, v92, v91
	v_add_u32_e32 v148, v95, v93
	v_add_u32_e32 v149, v98, v96
	v_add_u32_e32 v150, v100, v99
	v_add_u32_e32 v151, v102, v101
	v_add_u32_e32 v152, v104, v103
	v_add_u32_e32 v153, v106, v105
	v_add_u32_e32 v154, v108, v107
	v_add_u32_e32 v155, v109, v110
	v_add_u32_e32 v156, v112, v111
	v_add_u32_e32 v157, v114, v113
	v_add_u32_e32 v158, v115, v83
	v_add_u32_e32 v159, v80, v82
	v_add_u32_e32 v160, 64, v78
	v_mov_b32_e32 v96, 0xc604b4df
	v_mov_b32_e32 v95, v94
	v_mov_b32_e32 v98, v94
	v_mov_b32_e32 v99, v94
	v_mov_b32_e32 v100, v94
	v_mov_b32_e32 v101, v94
	v_mov_b32_e32 v102, v94
	v_mov_b32_e32 v103, v94
	v_mov_b32_e32 v104, v94
	v_mov_b32_e32 v105, v94
	v_mov_b32_e32 v106, v94
	v_mov_b32_e32 v107, v94
	v_mov_b32_e32 v108, v94
	v_mov_b32_e32 v109, v94
	v_mov_b32_e32 v110, v94
	v_mov_b32_e32 v111, v94
	v_mov_b32_e32 v112, v94
	v_mov_b32_e32 v113, v94
	v_mov_b32_e32 v114, v94
	v_mov_b32_e32 v115, v94
	v_mov_b32_e32 v117, v94
	s_waitcnt lgkmcnt(0)
	s_barrier
	s_mov_b32 s26, 0x2580
	s_mov_b32 s27, 0x3580
	s_mov_b32 s28, 0x4580
	buffer_load_dwordx4 v[6:9], v192, s[16:19], s26 offen nt
	buffer_load_dwordx4 v[10:13], v192, s[16:19], s26 offen offset:1024 nt
	buffer_load_dwordx4 v[18:21], v192, s[16:19], s26 offen offset:2048 nt
	buffer_load_dwordx4 v[22:25], v192, s[16:19], s26 offen offset:3072 nt
	buffer_load_dwordx4 v[26:29], v192, s[16:19], s27 offen nt
	buffer_load_dwordx4 v[30:33], v192, s[16:19], s27 offen offset:1024 nt
	buffer_load_dwordx4 v[38:41], v192, s[16:19], s27 offen offset:2048 nt
	buffer_load_dwordx4 v[42:45], v192, s[16:19], s27 offen offset:3072 nt
	buffer_load_dwordx4 v[50:53], v192, s[16:19], s28 offen nt
	buffer_load_dwordx4 v[186:189], v193, s[16:19], s26 offen offset:1024 nt
	s_waitcnt vmcnt(25)
	v_cvt_pk_f16_f32 v79, v4, v5
	v_cvt_pk_f16_f32 v78, v2, v3
	ds_write_b64 v141, v[78:79] offset:19456
	s_waitcnt vmcnt(24)
	v_cvt_pk_f16_f32 v79, v16, v17
	v_cvt_pk_f16_f32 v78, v14, v15
	ds_write_b64 v143, v[78:79] offset:19456
	s_waitcnt vmcnt(23)
	v_cvt_pk_f16_f32 v79, v36, v37
	v_cvt_pk_f16_f32 v78, v34, v35
	ds_write_b64 v144, v[78:79] offset:19456
	s_waitcnt vmcnt(22)
	v_cvt_pk_f16_f32 v79, v48, v49
	v_cvt_pk_f16_f32 v78, v46, v47
	ds_write_b64 v145, v[78:79] offset:19456
	s_waitcnt vmcnt(21)
	v_cvt_pk_f16_f32 v79, v56, v57
	v_cvt_pk_f16_f32 v78, v54, v55
	ds_write_b64 v146, v[78:79] offset:19456
	s_waitcnt vmcnt(20)
	v_cvt_pk_f16_f32 v79, v60, v61
	v_cvt_pk_f16_f32 v78, v58, v59
	ds_write_b64 v147, v[78:79] offset:19456
	s_waitcnt vmcnt(19)
	v_cvt_pk_f16_f32 v79, v64, v65
	v_cvt_pk_f16_f32 v78, v62, v63
	ds_write_b64 v141, v[78:79] offset:22568
	s_waitcnt vmcnt(18)
	v_cvt_pk_f16_f32 v79, v68, v69
	v_cvt_pk_f16_f32 v78, v66, v67
	ds_write_b64 v148, v[78:79] offset:19456
	s_waitcnt vmcnt(17)
	v_cvt_pk_f16_f32 v79, v72, v73
	v_cvt_pk_f16_f32 v78, v70, v71
	ds_write_b64 v149, v[78:79] offset:19456
	s_waitcnt vmcnt(16)
	v_cvt_pk_f16_f32 v79, v76, v77
	v_cvt_pk_f16_f32 v78, v74, v75
	s_and_saveexec_b64 s[12:13], s[8:9]
	ds_write_b64 v150, v[78:79] offset:19456
	s_or_b64 exec, exec, s[12:13]
	s_waitcnt vmcnt(10)
	v_cmp_lt_i32_e64 s[30:31], 1, v125
	v_cmp_lt_i32_e64 s[32:33], 1, v190
	v_cmp_lt_i32_e64 s[34:35], 1, v126
	v_cmp_lt_i32_e64 s[36:37], 1, v127
	v_cndmask_b32_e64 v191, 0, 1, s[30:31]
	v_cndmask_b32_e64 v190, 0, 2, s[32:33]
	v_cndmask_b32_e64 v126, 0, 4, s[34:35]
	v_cndmask_b32_e64 v127, 0, 8, s[36:37]
	v_or3_b32 v191, v191, v190, v126
	v_or_b32_e32 v191, v191, v127
	s_mov_b32 s26, 0x4b00
	s_mov_b32 s27, 0x5b00
	s_mov_b32 s28, 0x6b00
	buffer_load_dwordx4 v[2:5], v192, s[16:19], s26 offen nt
	buffer_load_dwordx4 v[14:17], v192, s[16:19], s26 offen offset:1024 nt
	buffer_load_dwordx4 v[34:37], v192, s[16:19], s26 offen offset:2048 nt
	buffer_load_dwordx4 v[46:49], v192, s[16:19], s26 offen offset:3072 nt
	buffer_load_dwordx4 v[54:57], v192, s[16:19], s27 offen nt
	buffer_load_dwordx4 v[58:61], v192, s[16:19], s27 offen offset:1024 nt
	buffer_load_dwordx4 v[62:65], v192, s[16:19], s27 offen offset:2048 nt
	buffer_load_dwordx4 v[66:69], v192, s[16:19], s27 offen offset:3072 nt
	buffer_load_dwordx4 v[70:73], v192, s[16:19], s28 offen nt
	buffer_load_dwordx4 v[74:77], v193, s[16:19], s26 offen offset:1024 nt
	s_mov_b32 s3, 0
	s_branch .LBB0_7
